# baseline (speedup 1.0000x reference)
.Lm_steps:
	s_waitcnt lgkmcnt(4)
	v_mfma_f32_32x32x16_f16 v[64:79], v[92:95], v[8:11], 0
	ds_read_b128 v[88:91], v128 offset:26624
	ds_read_b128 v[112:115], v128 offset:4096
	ds_read_b128 v[120:123], v128 offset:6144
	v_exp_f32_e32 v48, v48
	v_exp_f32_e32 v49, v49
	v_exp_f32_e32 v50, v50
	v_exp_f32_e32 v51, v51
	v_exp_f32_e32 v52, v52
	v_exp_f32_e32 v53, v53
	v_exp_f32_e32 v54, v54
	v_exp_f32_e32 v55, v55
	v_cvt_pk_bf16_f32 v80, v48, v49
	v_cvt_pk_bf16_f32 v81, v50, v51
	v_cvt_pk_bf16_f32 v82, v52, v53
	v_cvt_pk_bf16_f32 v83, v54, v55
	ds_read_b128 v[116:119], v128 offset:5120
	ds_read_b128 v[124:127], v128 offset:7168
	v_exp_f32_e32 v56, v56
	v_exp_f32_e32 v57, v57
	v_exp_f32_e32 v58, v58
	v_exp_f32_e32 v59, v59
	s_waitcnt lgkmcnt(7)
	v_mfma_f32_32x32x16_bf16 v[16:31], v[96:99], v[80:83], v[16:31]
	v_exp_f32_e32 v60, v60
	v_exp_f32_e32 v61, v61
	v_exp_f32_e32 v62, v62
	v_exp_f32_e32 v63, v63
	v_mfma_f32_32x32x16_bf16 v[32:47], v[104:107], v[80:83], v[32:47]
	v_cvt_pk_bf16_f32 v84, v56, v57
	v_cvt_pk_bf16_f32 v85, v58, v59
	v_cvt_pk_bf16_f32 v86, v60, v61
	v_cvt_pk_bf16_f32 v87, v62, v63
.Lm_after0:
.Lm_steps1:
	s_waitcnt lgkmcnt(4)
	v_mfma_f32_32x32x16_f16 v[48:63], v[88:91], v[8:11], 0
	ds_read_b128 v[92:95], v128 offset:27648
	ds_read_b128 v[96:99], v128 offset:8192
	ds_read_b128 v[104:107], v128 offset:10240
	v_exp_f32_e32 v64, v64
	v_exp_f32_e32 v65, v65
	v_exp_f32_e32 v66, v66
	v_exp_f32_e32 v67, v67
	v_mfma_f32_32x32x16_bf16 v[16:31], v[100:103], v[84:87], v[16:31]
	v_exp_f32_e32 v68, v68
	v_exp_f32_e32 v69, v69
	v_exp_f32_e32 v70, v70
	v_exp_f32_e32 v71, v71
	v_mfma_f32_32x32x16_bf16 v[32:47], v[108:111], v[84:87], v[32:47]
	v_cvt_pk_bf16_f32 v80, v64, v65
	v_cvt_pk_bf16_f32 v81, v66, v67
	v_cvt_pk_bf16_f32 v82, v68, v69
	v_cvt_pk_bf16_f32 v83, v70, v71
	ds_read_b128 v[100:103], v128 offset:9216
	ds_read_b128 v[108:111], v128 offset:11264
	v_exp_f32_e32 v72, v72
	v_exp_f32_e32 v73, v73
	v_exp_f32_e32 v74, v74
	v_exp_f32_e32 v75, v75
	s_waitcnt lgkmcnt(7)
	v_mfma_f32_32x32x16_bf16 v[16:31], v[112:115], v[80:83], v[16:31]
	v_exp_f32_e32 v76, v76
	v_exp_f32_e32 v77, v77
	v_exp_f32_e32 v78, v78
	v_exp_f32_e32 v79, v79
	v_mfma_f32_32x32x16_bf16 v[32:47], v[120:123], v[80:83], v[32:47]
	v_cvt_pk_bf16_f32 v84, v72, v73
	v_cvt_pk_bf16_f32 v85, v74, v75
	v_cvt_pk_bf16_f32 v86, v76, v77
	v_cvt_pk_bf16_f32 v87, v78, v79
	s_waitcnt lgkmcnt(4)
	v_mfma_f32_32x32x16_f16 v[64:79], v[92:95], v[8:11], 0
	ds_read_b128 v[88:91], v128 offset:28672
	ds_read_b128 v[112:115], v128 offset:12288
	ds_read_b128 v[120:123], v128 offset:14336
	v_exp_f32_e32 v48, v48
	v_exp_f32_e32 v49, v49
	v_exp_f32_e32 v50, v50
	v_exp_f32_e32 v51, v51
	v_mfma_f32_32x32x16_bf16 v[16:31], v[116:119], v[84:87], v[16:31]
	v_exp_f32_e32 v52, v52
	v_exp_f32_e32 v53, v53
	v_exp_f32_e32 v54, v54
	v_exp_f32_e32 v55, v55
	v_mfma_f32_32x32x16_bf16 v[32:47], v[124:127], v[84:87], v[32:47]
	v_cvt_pk_bf16_f32 v80, v48, v49
	v_cvt_pk_bf16_f32 v81, v50, v51
	v_cvt_pk_bf16_f32 v82, v52, v53
	v_cvt_pk_bf16_f32 v83, v54, v55
	ds_read_b128 v[116:119], v128 offset:13312
	ds_read_b128 v[124:127], v128 offset:15360
	v_exp_f32_e32 v56, v56
	v_exp_f32_e32 v57, v57
	v_exp_f32_e32 v58, v58
	v_exp_f32_e32 v59, v59
	s_waitcnt lgkmcnt(7)
	v_mfma_f32_32x32x16_bf16 v[16:31], v[96:99], v[80:83], v[16:31]
	v_exp_f32_e32 v60, v60
	v_exp_f32_e32 v61, v61
	v_exp_f32_e32 v62, v62
	v_exp_f32_e32 v63, v63
	v_mfma_f32_32x32x16_bf16 v[32:47], v[104:107], v[80:83], v[32:47]
	v_cvt_pk_bf16_f32 v84, v56, v57
	v_cvt_pk_bf16_f32 v85, v58, v59
	v_cvt_pk_bf16_f32 v86, v60, v61
	v_cvt_pk_bf16_f32 v87, v62, v63
	s_waitcnt lgkmcnt(4)
	v_mfma_f32_32x32x16_f16 v[48:63], v[88:91], v[8:11], 0
	ds_read_b128 v[92:95], v128 offset:29696
	ds_read_b128 v[96:99], v128 offset:16384
	ds_read_b128 v[104:107], v128 offset:18432
	v_exp_f32_e32 v64, v64
	v_exp_f32_e32 v65, v65
	v_exp_f32_e32 v66, v66
	v_exp_f32_e32 v67, v67
	v_mfma_f32_32x32x16_bf16 v[16:31], v[100:103], v[84:87], v[16:31]
	v_exp_f32_e32 v68, v68
	v_exp_f32_e32 v69, v69
	v_exp_f32_e32 v70, v70
	v_exp_f32_e32 v71, v71
	v_mfma_f32_32x32x16_bf16 v[32:47], v[108:111], v[84:87], v[32:47]
	v_cvt_pk_bf16_f32 v80, v64, v65
	v_cvt_pk_bf16_f32 v81, v66, v67
	v_cvt_pk_bf16_f32 v82, v68, v69
	v_cvt_pk_bf16_f32 v83, v70, v71
	ds_read_b128 v[100:103], v128 offset:17408
	ds_read_b128 v[108:111], v128 offset:19456
	v_exp_f32_e32 v72, v72
	v_exp_f32_e32 v73, v73
	v_exp_f32_e32 v74, v74
	v_exp_f32_e32 v75, v75
	s_waitcnt lgkmcnt(7)
	v_mfma_f32_32x32x16_bf16 v[16:31], v[112:115], v[80:83], v[16:31]
	v_exp_f32_e32 v76, v76
	v_exp_f32_e32 v77, v77
	v_exp_f32_e32 v78, v78
	v_exp_f32_e32 v79, v79
	v_mfma_f32_32x32x16_bf16 v[32:47], v[120:123], v[80:83], v[32:47]
	v_cvt_pk_bf16_f32 v84, v72, v73
	v_cvt_pk_bf16_f32 v85, v74, v75
	v_cvt_pk_bf16_f32 v86, v76, v77
	v_cvt_pk_bf16_f32 v87, v78, v79
	s_waitcnt lgkmcnt(4)
	v_mfma_f32_32x32x16_f16 v[64:79], v[92:95], v[8:11], 0
	ds_read_b128 v[88:91], v129 offset:24576
	ds_read_b128 v[112:115], v128 offset:20480
	ds_read_b128 v[120:123], v128 offset:22528
	v_exp_f32_e32 v48, v48
	v_exp_f32_e32 v49, v49
	v_exp_f32_e32 v50, v50
	v_exp_f32_e32 v51, v51
	v_mfma_f32_32x32x16_bf16 v[16:31], v[116:119], v[84:87], v[16:31]
	v_exp_f32_e32 v52, v52
	v_exp_f32_e32 v53, v53
	v_exp_f32_e32 v54, v54
	v_exp_f32_e32 v55, v55
	v_mfma_f32_32x32x16_bf16 v[32:47], v[124:127], v[84:87], v[32:47]
	v_cvt_pk_bf16_f32 v80, v48, v49
	v_cvt_pk_bf16_f32 v81, v50, v51
	v_cvt_pk_bf16_f32 v82, v52, v53
	v_cvt_pk_bf16_f32 v83, v54, v55
	ds_read_b128 v[116:119], v128 offset:21504
	ds_read_b128 v[124:127], v128 offset:23552
	v_exp_f32_e32 v56, v56
	v_exp_f32_e32 v57, v57
	v_exp_f32_e32 v58, v58
	v_exp_f32_e32 v59, v59
	s_waitcnt lgkmcnt(7)
	v_mfma_f32_32x32x16_bf16 v[16:31], v[96:99], v[80:83], v[16:31]
	v_exp_f32_e32 v60, v60
	v_exp_f32_e32 v61, v61
	v_exp_f32_e32 v62, v62
	v_exp_f32_e32 v63, v63
	v_mfma_f32_32x32x16_bf16 v[32:47], v[104:107], v[80:83], v[32:47]
	v_cvt_pk_bf16_f32 v84, v56, v57
	v_cvt_pk_bf16_f32 v85, v58, v59
	v_cvt_pk_bf16_f32 v86, v60, v61
	v_cvt_pk_bf16_f32 v87, v62, v63
	s_waitcnt lgkmcnt(4)
	v_mfma_f32_32x32x16_f16 v[48:63], v[88:91], v[8:11], 0
	ds_read_b128 v[92:95], v129 offset:25600
	s_add_u32 s28, s27, 3
	ds_read_b128 v[96:99], v129 offset:0
	s_sub_u32 s30, s28, s25
	ds_read_b128 v[104:107], v129 offset:2048
	s_mul_i32 s30, s30, 6
	v_exp_f32_e32 v64, v64
	s_add_u32 s30, s30, s24
	v_exp_f32_e32 v65, v65
	s_mul_i32 s31, s28, 6
	v_exp_f32_e32 v66, v66
	s_add_u32 s31, s31, s22
	v_exp_f32_e32 v67, v67
	s_cmp_lt_u32 s28, s25
	v_mfma_f32_32x32x16_bf16 v[16:31], v[100:103], v[84:87], v[16:31]
	s_cselect_b32 s30, s31, s30
	v_exp_f32_e32 v68, v68
	s_lshl_b32 s33, s18, 10
	v_exp_f32_e32 v69, v69
	s_lshl_b32 s31, s30, 12
	v_exp_f32_e32 v70, v70
	s_add_u32 s31, s31, s33
	v_exp_f32_e32 v71, v71
	s_add_u32 s50, s8, s31
	v_mfma_f32_32x32x16_bf16 v[32:47], v[108:111], v[84:87], v[32:47]
	s_addc_u32 s51, s9, 0
	v_cvt_pk_bf16_f32 v80, v64, v65
	s_add_u32 s52, s50, 0x3000
	v_cvt_pk_bf16_f32 v81, v66, v67
	s_addc_u32 s53, s51, 0
	v_cvt_pk_bf16_f32 v82, v68, v69
	s_lshl_b32 s31, s30, 10
	v_cvt_pk_bf16_f32 v83, v70, v71
	s_add_u32 s31, s31, s33
	ds_read_b128 v[100:103], v129 offset:1024
	s_sub_u32 s31, s31, 0
	ds_read_b128 v[108:111], v129 offset:3072
	s_add_u32 s54, s4, s31
	v_exp_f32_e32 v72, v72
	s_addc_u32 s55, s5, 0
	v_exp_f32_e32 v73, v73
	s_add_u32 s34, s46, s33
	v_exp_f32_e32 v74, v74
	s_add_u32 s35, s34, 0x3000
	v_exp_f32_e32 v75, v75
	s_add_u32 s36, s34, 24576
	s_waitcnt lgkmcnt(7)
	v_mfma_f32_32x32x16_bf16 v[16:31], v[112:115], v[80:83], v[16:31]
	v_exp_f32_e32 v76, v76
	v_exp_f32_e32 v77, v77
	v_exp_f32_e32 v78, v78
	v_exp_f32_e32 v79, v79
	v_mfma_f32_32x32x16_bf16 v[32:47], v[120:123], v[80:83], v[32:47]
	v_cvt_pk_bf16_f32 v84, v72, v73
	v_cvt_pk_bf16_f32 v85, v74, v75
	v_cvt_pk_bf16_f32 v86, v76, v77
	v_cvt_pk_bf16_f32 v87, v78, v79
	s_waitcnt lgkmcnt(5)
	s_nop 0
	v_mfma_f32_32x32x16_bf16 v[16:31], v[116:119], v[84:87], v[16:31]
	v_mfma_f32_32x32x16_bf16 v[32:47], v[124:127], v[84:87], v[32:47]
	s_mov_b32 s30, s46
	s_mov_b32 s46, s47
	s_mov_b32 s47, s48
	s_mov_b32 s48, s30
	s_add_u32 s27, s27, 1
	s_cmp_lt_u32 s27, 9
	s_cbranch_scc0 .Lm_flush
	s_cmp_eq_u32 s27, s25
	s_cbranch_scc1 .Lm_flush
	s_waitcnt vmcnt(0)
.Lm_bar:
	s_barrier
	v_add_u32_e32 v128, s46, v2
	v_add_u32_e32 v129, s47, v2
	s_add_u32 s28, s27, 2
	s_cmp_lt_u32 s28, 9
	s_cbranch_scc0 .Lm_nod_lp
	s_mov_b32 m0, s34
	s_nop 0
	global_load_lds_dwordx4 v2, s[50:51]
	s_mov_b32 m0, s35
	s_nop 0
	global_load_lds_dwordx4 v2, s[52:53]
	s_cmp_lt_u32 s18, 6
	s_cbranch_scc0 .Lm_nod_lp
	s_mov_b32 m0, s36
	s_nop 0
	global_load_lds_dwordx4 v2, s[54:55]
